# union7 + GEMM K-loops (proj, out, up, down): the wave-uniform relax flag kept scalar (one s_and_b64 into the consumer mask) instead of the v_cndmask/v_readfirstlane/s_cmp/s_cselect round trip, 6 instr
# speedup vs baseline: 1.0052x; 1.0009x over previous
; #define PG8_STAGE(bufoff, gbase, voff) do { _Pragma("unroll") for (int _i = 0; _i < 2; ++_i) \
;         __builtin_amdgcn_global_load_lds((const unsigned*)((const char*)(gbase) + (voff)[_i]), (PG8_LAS unsigned*)(lds + (bufoff) + ldsw + _i * 8192), 16, 0, 0); } while (0)
; #define PG8_LDA(dst, b, h) do { _Pragma("unroll") for (int m = 0; m < 4; ++m) _Pragma("unroll") for (int k = 0; k < 2; ++k) dst[m][k] = *(const PG8_LAS bf16x8*)(lds + PG8_SA(b, h) + aoff + m * 2048 + k * 1024); } while (0)
; #define PG8_LDB(dst, b, h) do { _Pragma("unroll") for (int n = 0; n < 2; ++n) _Pragma("unroll") for (int k = 0; k < 2; ++k) dst[n][k] = *(const PG8_LAS bf16x8*)(lds + PG8_SB(b, h) + boff + n * 2048 + k * 1024); } while (0)
; #define PG8_MMA(ai, bj, At, Bt) do { __builtin_amdgcn_s_setprio(1); _Pragma("unroll") for (int m = 0; m < 4; ++m) _Pragma("unroll") for (int n = 0; n < 2; ++n) _Pragma("unroll") for (int k = 0; k < 2; ++k) \
;         acc[ai][bj][m][n] = mma16(Bt[n][k], At[m][k], acc[ai][bj][m][n]); __builtin_amdgcn_s_setprio(0); } while (0)
; #define PG8_WAIT_V(n) asm volatile("s_waitcnt vmcnt(" #n ")" ::: "memory")
; #define PG8_WAIT_VN(n) asm volatile("s_waitcnt vmcnt(%0)" :: "n"(n) : "memory")
; #define PG8_WAIT_L(n) asm volatile("s_waitcnt lgkmcnt(" #n ")" ::: "memory")
; #define PG8_BAR __builtin_amdgcn_s_barrier()
; #define PG8_SCHED __builtin_amdgcn_sched_barrier(0)
; template <class Epi, class Sched, bool ALIGN_EPI = false, bool SP2 = false>
; __device__ __forceinline__ void gemm_phase(PG8_LAS unsigned char* lds, const Gemm g, const Sched& S, const Epi& E, Stopwatch& sw) {
;     ...
;             int relax = __builtin_amdgcn_readfirstlane((int)((ui > 0) && (t == 0))); asm volatile("" : "+s"(relax));
;             PG8_LDB(B0, 0, 0); PG8_LDB(B1, 0, 1); PG8_SCHED; PG8_LDA(At, 0, 0); if (!relax) PG8_STAGE(PG8_SA(1, 1), a1 + hstep, voffA);
;             if (relax) PG8_WAIT_VN(8 + Epi::NST); else PG8_WAIT_V(8); PG8_WAIT_L(0); PG8_BAR; PG8_MMA(0, 0, At, B0); PG8_MMA(0, 1, At, B1); PG8_BAR; PG8_SCHED;
.LBB0_154:
	s_cmp_eq_u32 s60, 0
	s_cselect_b64 s[38:39], -1, 0
	s_and_b64 s[74:75], s[58:59], s[38:39]
	ds_read_b128 v[148:151], v228
	ds_read_b128 v[152:155], v228 offset:1024
	ds_read_b128 v[156:159], v228 offset:2048
	ds_read_b128 v[160:163], v228 offset:3072
	ds_read_b128 v[132:135], v229
	ds_read_b128 v[136:139], v229 offset:1024
	ds_read_b128 v[140:143], v229 offset:2048
	ds_read_b128 v[144:147], v229 offset:3072
	ds_read_b128 v[188:191], v230
	ds_read_b128 v[192:195], v230 offset:1024
	ds_read_b128 v[180:183], v230 offset:2048
	ds_read_b128 v[184:187], v230 offset:3072
	ds_read_b128 v[172:175], v230 offset:4096
	ds_read_b128 v[176:179], v230 offset:5120
	ds_read_b128 v[164:167], v230 offset:6144
	ds_read_b128 v[168:171], v230 offset:7168
	s_and_b64 vcc, exec, s[74:75]
	s_cbranch_vccz .LBB0_165
	s_waitcnt vmcnt(24)
	s_cbranch_execnz .LBB0_157

; #define PG8_STAGE(bufoff, gbase, voff) do { _Pragma("unroll") for (int _i = 0; _i < 2; ++_i) \
;         __builtin_amdgcn_global_load_lds((const unsigned*)((const char*)(gbase) + (voff)[_i]), (PG8_LAS unsigned*)(lds + (bufoff) + ldsw + _i * 8192), 16, 0, 0); } while (0)
; #define PG8_LDA(dst, b, h) do { _Pragma("unroll") for (int m = 0; m < 4; ++m) _Pragma("unroll") for (int k = 0; k < 2; ++k) dst[m][k] = *(const PG8_LAS bf16x8*)(lds + PG8_SA(b, h) + aoff + m * 2048 + k * 1024); } while (0)
; #define PG8_LDB(dst, b, h) do { _Pragma("unroll") for (int n = 0; n < 2; ++n) _Pragma("unroll") for (int k = 0; k < 2; ++k) dst[n][k] = *(const PG8_LAS bf16x8*)(lds + PG8_SB(b, h) + boff + n * 2048 + k * 1024); } while (0)
; #define PG8_MMA(ai, bj, At, Bt) do { __builtin_amdgcn_s_setprio(1); _Pragma("unroll") for (int m = 0; m < 4; ++m) _Pragma("unroll") for (int n = 0; n < 2; ++n) _Pragma("unroll") for (int k = 0; k < 2; ++k) \
;         acc[ai][bj][m][n] = mma16(Bt[n][k], At[m][k], acc[ai][bj][m][n]); __builtin_amdgcn_s_setprio(0); } while (0)
; #define PG8_WAIT_V(n) asm volatile("s_waitcnt vmcnt(" #n ")" ::: "memory")
; #define PG8_WAIT_VN(n) asm volatile("s_waitcnt vmcnt(%0)" :: "n"(n) : "memory")
; #define PG8_WAIT_L(n) asm volatile("s_waitcnt lgkmcnt(" #n ")" ::: "memory")
; #define PG8_BAR __builtin_amdgcn_s_barrier()
; #define PG8_SCHED __builtin_amdgcn_sched_barrier(0)
; template <class Epi, class Sched, bool ALIGN_EPI = false, bool SP2 = false>
; __device__ __forceinline__ void gemm_phase(PG8_LAS unsigned char* lds, const Gemm g, const Sched& S, const Epi& E, Stopwatch& sw) {
;     ...
;             int relax = __builtin_amdgcn_readfirstlane((int)((ui > 0) && (t == 0))); asm volatile("" : "+s"(relax));
;             PG8_LDB(B0, 0, 0); PG8_LDB(B1, 0, 1); PG8_SCHED; PG8_LDA(At, 0, 0); if (!relax) PG8_STAGE(PG8_SA(1, 1), a1 + hstep, voffA);
;             if (relax) PG8_WAIT_VN(8 + Epi::NST); else PG8_WAIT_V(8); PG8_WAIT_L(0); PG8_BAR; PG8_MMA(0, 0, At, B0); PG8_MMA(0, 1, At, B1); PG8_BAR; PG8_SCHED;
.LBB0_890:
	s_cmp_eq_u32 s62, 0
	s_cselect_b64 s[42:43], -1, 0
	s_and_b64 s[78:79], s[60:61], s[42:43]
	v_add_u32_e32 v144, 0x14000, v227
	v_add_u32_e32 v132, 0x10000, v227
	ds_read_b128 v[148:151], v132
	ds_read_b128 v[152:155], v132 offset:1024
	ds_read_b128 v[156:159], v132 offset:2048
	ds_read_b128 v[160:163], v132 offset:3072
	ds_read_b128 v[132:135], v144
	ds_read_b128 v[136:139], v144 offset:1024
	ds_read_b128 v[140:143], v144 offset:2048
	ds_read_b128 v[144:147], v144 offset:3072
	ds_read_b128 v[188:191], v228
	ds_read_b128 v[192:195], v228 offset:1024
	ds_read_b128 v[180:183], v228 offset:2048
	ds_read_b128 v[184:187], v228 offset:3072
	ds_read_b128 v[172:175], v228 offset:4096
	ds_read_b128 v[176:179], v228 offset:5120
	ds_read_b128 v[164:167], v228 offset:6144
	ds_read_b128 v[168:171], v228 offset:7168
	s_and_b64 vcc, exec, s[78:79]
	s_cbranch_vccz .LBB0_901
	s_waitcnt vmcnt(32)
	s_cbranch_execnz .LBB0_893

; #define PG8_STAGE(bufoff, gbase, voff) do { _Pragma("unroll") for (int _i = 0; _i < 2; ++_i) \
;         __builtin_amdgcn_global_load_lds((const unsigned*)((const char*)(gbase) + (voff)[_i]), (PG8_LAS unsigned*)(lds + (bufoff) + ldsw + _i * 8192), 16, 0, 0); } while (0)
; #define PG8_LDA(dst, b, h) do { _Pragma("unroll") for (int m = 0; m < 4; ++m) _Pragma("unroll") for (int k = 0; k < 2; ++k) dst[m][k] = *(const PG8_LAS bf16x8*)(lds + PG8_SA(b, h) + aoff + m * 2048 + k * 1024); } while (0)
; #define PG8_LDB(dst, b, h) do { _Pragma("unroll") for (int n = 0; n < 2; ++n) _Pragma("unroll") for (int k = 0; k < 2; ++k) dst[n][k] = *(const PG8_LAS bf16x8*)(lds + PG8_SB(b, h) + boff + n * 2048 + k * 1024); } while (0)
; #define PG8_MMA(ai, bj, At, Bt) do { __builtin_amdgcn_s_setprio(1); _Pragma("unroll") for (int m = 0; m < 4; ++m) _Pragma("unroll") for (int n = 0; n < 2; ++n) _Pragma("unroll") for (int k = 0; k < 2; ++k) \
;         acc[ai][bj][m][n] = mma16(Bt[n][k], At[m][k], acc[ai][bj][m][n]); __builtin_amdgcn_s_setprio(0); } while (0)
; #define PG8_WAIT_V(n) asm volatile("s_waitcnt vmcnt(" #n ")" ::: "memory")
; #define PG8_WAIT_VN(n) asm volatile("s_waitcnt vmcnt(%0)" :: "n"(n) : "memory")
; #define PG8_WAIT_L(n) asm volatile("s_waitcnt lgkmcnt(" #n ")" ::: "memory")
; #define PG8_BAR __builtin_amdgcn_s_barrier()
; #define PG8_SCHED __builtin_amdgcn_sched_barrier(0)
; template <class Epi, class Sched, bool ALIGN_EPI = false, bool SP2 = false>
; __device__ __forceinline__ void gemm_phase(PG8_LAS unsigned char* lds, const Gemm g, const Sched& S, const Epi& E, Stopwatch& sw) {
;     ...
;             int relax = __builtin_amdgcn_readfirstlane((int)((ui > 0) && (t == 0))); asm volatile("" : "+s"(relax));
;             PG8_LDB(B0, 0, 0); PG8_LDB(B1, 0, 1); PG8_SCHED; PG8_LDA(At, 0, 0); if (!relax) PG8_STAGE(PG8_SA(1, 1), a1 + hstep, voffA);
;             if (relax) PG8_WAIT_VN(8 + Epi::NST); else PG8_WAIT_V(8); PG8_WAIT_L(0); PG8_BAR; PG8_MMA(0, 0, At, B0); PG8_MMA(0, 1, At, B1); PG8_BAR; PG8_SCHED;
.LBB0_1118:
	s_cmp_eq_u32 s62, 0
	s_cselect_b64 s[40:41], -1, 0
	s_and_b64 s[78:79], s[60:61], s[40:41]
	v_add_u32_e32 v144, 0x11000, v227
	v_add_u32_e32 v132, 0x10000, v227
	ds_read_b128 v[148:151], v132
	ds_read_b128 v[152:155], v132 offset:1024
	ds_read_b128 v[156:159], v132 offset:2048
	ds_read_b128 v[160:163], v132 offset:3072
	ds_read_b128 v[132:135], v144
	ds_read_b128 v[136:139], v144 offset:1024
	ds_read_b128 v[140:143], v144 offset:2048
	ds_read_b128 v[144:147], v144 offset:3072
	ds_read_b128 v[188:191], v228
	ds_read_b128 v[192:195], v228 offset:1024
	ds_read_b128 v[180:183], v228 offset:2048
	ds_read_b128 v[184:187], v228 offset:3072
	ds_read_b128 v[172:175], v228 offset:4096
	ds_read_b128 v[176:179], v228 offset:5120
	ds_read_b128 v[164:167], v228 offset:6144
	ds_read_b128 v[168:171], v228 offset:7168
	s_and_b64 vcc, exec, s[78:79]
	s_cbranch_vccz .LBB0_1129
	s_waitcnt vmcnt(24)
	s_cbranch_execnz .LBB0_1121

; #define PG8_STAGE(bufoff, gbase, voff) do { _Pragma("unroll") for (int _i = 0; _i < 2; ++_i) \
;         __builtin_amdgcn_global_load_lds((const unsigned*)((const char*)(gbase) + (voff)[_i]), (PG8_LAS unsigned*)(lds + (bufoff) + ldsw + _i * 8192), 16, 0, 0); } while (0)
; #define PG8_LDA(dst, b, h) do { _Pragma("unroll") for (int m = 0; m < 4; ++m) _Pragma("unroll") for (int k = 0; k < 2; ++k) dst[m][k] = *(const PG8_LAS bf16x8*)(lds + PG8_SA(b, h) + aoff + m * 2048 + k * 1024); } while (0)
; #define PG8_LDB(dst, b, h) do { _Pragma("unroll") for (int n = 0; n < 2; ++n) _Pragma("unroll") for (int k = 0; k < 2; ++k) dst[n][k] = *(const PG8_LAS bf16x8*)(lds + PG8_SB(b, h) + boff + n * 2048 + k * 1024); } while (0)
; #define PG8_MMA(ai, bj, At, Bt) do { __builtin_amdgcn_s_setprio(1); _Pragma("unroll") for (int m = 0; m < 4; ++m) _Pragma("unroll") for (int n = 0; n < 2; ++n) _Pragma("unroll") for (int k = 0; k < 2; ++k) \
;         acc[ai][bj][m][n] = mma16(Bt[n][k], At[m][k], acc[ai][bj][m][n]); __builtin_amdgcn_s_setprio(0); } while (0)
; #define PG8_WAIT_V(n) asm volatile("s_waitcnt vmcnt(" #n ")" ::: "memory")
; #define PG8_WAIT_VN(n) asm volatile("s_waitcnt vmcnt(%0)" :: "n"(n) : "memory")
; #define PG8_WAIT_L(n) asm volatile("s_waitcnt lgkmcnt(" #n ")" ::: "memory")
; #define PG8_BAR __builtin_amdgcn_s_barrier()
; #define PG8_SCHED __builtin_amdgcn_sched_barrier(0)
; template <class Epi, class Sched, bool ALIGN_EPI = false, bool SP2 = false>
; __device__ __forceinline__ void gemm_phase(PG8_LAS unsigned char* lds, const Gemm g, const Sched& S, const Epi& E, Stopwatch& sw) {
;     ...
;             int relax = __builtin_amdgcn_readfirstlane((int)((ui > 0) && (t == 0))); asm volatile("" : "+s"(relax));
;             PG8_LDB(B0, 0, 0); PG8_LDB(B1, 0, 1); PG8_SCHED; PG8_LDA(At, 0, 0); if (!relax) PG8_STAGE(PG8_SA(1, 1), a1 + hstep, voffA);
;             if (relax) PG8_WAIT_VN(8 + Epi::NST); else PG8_WAIT_V(8); PG8_WAIT_L(0); PG8_BAR; PG8_MMA(0, 0, At, B0); PG8_MMA(0, 1, At, B1); PG8_BAR; PG8_SCHED;
.LBB0_1228:
	s_cmp_eq_u32 s60, 0
	s_cselect_b64 s[40:41], -1, 0
	s_and_b64 s[74:75], s[58:59], s[40:41]
	v_add_u32_e32 v144, 0x14000, v227
	v_add_u32_e32 v132, 0x10000, v227
	ds_read_b128 v[148:151], v132
	ds_read_b128 v[152:155], v132 offset:1024
	ds_read_b128 v[156:159], v132 offset:2048
	ds_read_b128 v[160:163], v132 offset:3072
	ds_read_b128 v[132:135], v144
	ds_read_b128 v[136:139], v144 offset:1024
	ds_read_b128 v[140:143], v144 offset:2048
	ds_read_b128 v[144:147], v144 offset:3072
	ds_read_b128 v[188:191], v228
	ds_read_b128 v[192:195], v228 offset:1024
	ds_read_b128 v[180:183], v228 offset:2048
	ds_read_b128 v[184:187], v228 offset:3072
	ds_read_b128 v[172:175], v228 offset:4096
	ds_read_b128 v[176:179], v228 offset:5120
	ds_read_b128 v[164:167], v228 offset:6144
	ds_read_b128 v[168:171], v228 offset:7168
	s_and_b64 vcc, exec, s[74:75]
	s_cbranch_vccz .LBB0_1239
	s_waitcnt vmcnt(32)
	s_cbranch_execnz .LBB0_1231
